# v26 with sc0 sc1 nt (instead of nt) on P0's expert f32 loads
# baseline (speedup 1.0000x reference)
; #define MOE_LOAD(v, it) do { _Pragma("unroll") for (int i_ = 0; i_ < 64; ++i_) v[i_] = __builtin_nontemporal_load((it).src + (size_t)(2 * i_) * (it).stride); } while (0)
;     ...
;         const int nmine = (NMOE - gw + NGW - 1) / NGW;
;         const int last = gw + (nmine - 1) * NGW;
;         MoeItem ia = moe_item(wg, wu, wd, win, wout, wpn, wpd, F.ws, gw, F.lane), ib = ia;
;         MOE_LOAD(va, ia);
.LBB0_77:
	s_mul_i32 s5, s47, s6
	s_sub_i32 s5, s7, s5
	s_xor_b32 s4, s68, s4
	s_add_i32 s7, s47, 1
	s_sub_i32 s43, s5, s6
	s_cmp_ge_u32 s5, s6
	s_cselect_b32 s7, s7, s47
	s_cselect_b32 s5, s43, s5
	s_add_i32 s43, s7, 1
	s_cmp_ge_u32 s5, s6
	s_cselect_b32 s5, s43, s7
	s_xor_b32 s5, s5, s4
	s_sub_i32 s6, s5, s4
	s_cmp_lt_i32 s6, 1
	s_cbranch_scc1 .LBB0_130
	s_add_i32 s4, s6, -1
	s_mul_i32 s7, s4, s72
	s_add_i32 s7, s7, s3
	s_mul_i32 s4, s44, 0x1f8
	s_lshl_b64 s[44:45], s[44:45], 3
	s_mov_b32 s5, 0
	s_sub_u32 s44, 0, s44
	v_lshl_add_u64 v[8:9], v[4:5], 0, s[4:5]
	s_subb_u32 s45, 0, s45
	v_lshl_add_u64 v[10:11], v[8:9], 0, s[44:45]
	v_lshl_add_u64 v[12:13], v[10:11], 0, s[44:45]
	v_lshl_add_u64 v[14:15], v[12:13], 0, s[44:45]
	v_lshl_add_u64 v[16:17], v[14:15], 0, s[44:45]
	v_lshl_add_u64 v[18:19], v[16:17], 0, s[44:45]
	v_lshl_add_u64 v[20:21], v[18:19], 0, s[44:45]
	v_lshl_add_u64 v[22:23], v[20:21], 0, s[44:45]
	global_load_dword v50, v[8:9], off sc0 sc1 nt
	global_load_dword v49, v[10:11], off sc0 sc1 nt
	global_load_dword v48, v[12:13], off sc0 sc1 nt
	global_load_dword v47, v[14:15], off sc0 sc1 nt
	global_load_dword v44, v[16:17], off sc0 sc1 nt
	global_load_dword v43, v[18:19], off sc0 sc1 nt
	global_load_dword v41, v[20:21], off sc0 sc1 nt
	global_load_dword v37, v[22:23], off sc0 sc1 nt
	v_lshl_add_u64 v[8:9], v[22:23], 0, s[44:45]
	v_lshl_add_u64 v[10:11], v[8:9], 0, s[44:45]
	global_load_dword v42, v[8:9], off sc0 sc1 nt
	global_load_dword v40, v[10:11], off sc0 sc1 nt
	v_lshl_add_u64 v[8:9], v[10:11], 0, s[44:45]
	global_load_dword v39, v[8:9], off sc0 sc1 nt
	v_lshl_add_u64 v[8:9], v[8:9], 0, s[44:45]
	global_load_dword v38, v[8:9], off sc0 sc1 nt
	v_lshl_add_u64 v[8:9], v[8:9], 0, s[44:45]
	global_load_dword v52, v[8:9], off sc0 sc1 nt
	v_lshl_add_u64 v[8:9], v[8:9], 0, s[44:45]
	global_load_dword v51, v[8:9], off sc0 sc1 nt
	v_lshl_add_u64 v[8:9], v[8:9], 0, s[44:45]
	global_load_dword v56, v[8:9], off sc0 sc1 nt
	v_lshl_add_u64 v[8:9], v[8:9], 0, s[44:45]
	global_load_dword v55, v[8:9], off sc0 sc1 nt
	v_lshl_add_u64 v[8:9], v[8:9], 0, s[44:45]
	global_load_dword v60, v[8:9], off sc0 sc1 nt
	v_lshl_add_u64 v[8:9], v[8:9], 0, s[44:45]
	global_load_dword v59, v[8:9], off sc0 sc1 nt
	v_lshl_add_u64 v[8:9], v[8:9], 0, s[44:45]
	global_load_dword v64, v[8:9], off sc0 sc1 nt
	v_lshl_add_u64 v[8:9], v[8:9], 0, s[44:45]
	global_load_dword v63, v[8:9], off sc0 sc1 nt
	v_lshl_add_u64 v[8:9], v[8:9], 0, s[44:45]
	global_load_dword v68, v[8:9], off sc0 sc1 nt
	v_lshl_add_u64 v[8:9], v[8:9], 0, s[44:45]
	global_load_dword v67, v[8:9], off sc0 sc1 nt
	v_lshl_add_u64 v[8:9], v[8:9], 0, s[44:45]
	global_load_dword v70, v[8:9], off sc0 sc1 nt
	v_lshl_add_u64 v[8:9], v[8:9], 0, s[44:45]
	global_load_dword v69, v[8:9], off sc0 sc1 nt
	v_lshl_add_u64 v[8:9], v[8:9], 0, s[44:45]
	global_load_dword v74, v[8:9], off sc0 sc1 nt
	v_lshl_add_u64 v[8:9], v[8:9], 0, s[44:45]
	global_load_dword v73, v[8:9], off sc0 sc1 nt
	v_lshl_add_u64 v[8:9], v[8:9], 0, s[44:45]
	global_load_dword v78, v[8:9], off sc0 sc1 nt
	v_lshl_add_u64 v[8:9], v[8:9], 0, s[44:45]
	global_load_dword v77, v[8:9], off sc0 sc1 nt
	v_lshl_add_u64 v[8:9], v[8:9], 0, s[44:45]
	global_load_dword v82, v[8:9], off sc0 sc1 nt
	v_lshl_add_u64 v[8:9], v[8:9], 0, s[44:45]
	global_load_dword v81, v[8:9], off sc0 sc1 nt
	v_lshl_add_u64 v[8:9], v[8:9], 0, s[44:45]
	global_load_dword v30, v[8:9], off sc0 sc1 nt
	v_lshl_add_u64 v[8:9], v[8:9], 0, s[44:45]
	global_load_dword v29, v[8:9], off sc0 sc1 nt
	v_lshl_add_u64 v[8:9], v[8:9], 0, s[44:45]
	global_load_dword v32, v[8:9], off sc0 sc1 nt
	v_lshl_add_u64 v[8:9], v[8:9], 0, s[44:45]
	global_load_dword v31, v[8:9], off sc0 sc1 nt
	v_lshl_add_u64 v[8:9], v[8:9], 0, s[44:45]
	global_load_dword v34, v[8:9], off sc0 sc1 nt
	v_lshl_add_u64 v[8:9], v[8:9], 0, s[44:45]
	global_load_dword v33, v[8:9], off sc0 sc1 nt
	v_lshl_add_u64 v[8:9], v[8:9], 0, s[44:45]
; #define MOE_LOAD(v, it) do { _Pragma("unroll") for (int i_ = 0; i_ < 64; ++i_) v[i_] = __builtin_nontemporal_load((it).src + (size_t)(2 * i_) * (it).stride); } while (0)
;     ...
;         MOE_LOAD(va, ia);
	global_load_dword v36, v[8:9], off sc0 sc1 nt
	v_lshl_add_u64 v[8:9], v[8:9], 0, s[44:45]
	global_load_dword v35, v[8:9], off sc0 sc1 nt
	v_lshl_add_u64 v[8:9], v[8:9], 0, s[44:45]
	global_load_dword v46, v[8:9], off sc0 sc1 nt
	v_lshl_add_u64 v[8:9], v[8:9], 0, s[44:45]
	global_load_dword v45, v[8:9], off sc0 sc1 nt
	v_lshl_add_u64 v[8:9], v[8:9], 0, s[44:45]
	global_load_dword v54, v[8:9], off sc0 sc1 nt
	v_lshl_add_u64 v[8:9], v[8:9], 0, s[44:45]
	global_load_dword v53, v[8:9], off sc0 sc1 nt
	v_lshl_add_u64 v[8:9], v[8:9], 0, s[44:45]
	global_load_dword v58, v[8:9], off sc0 sc1 nt
	v_lshl_add_u64 v[8:9], v[8:9], 0, s[44:45]
	global_load_dword v57, v[8:9], off sc0 sc1 nt
	v_lshl_add_u64 v[8:9], v[8:9], 0, s[44:45]
	global_load_dword v62, v[8:9], off sc0 sc1 nt
	v_lshl_add_u64 v[8:9], v[8:9], 0, s[44:45]
	global_load_dword v61, v[8:9], off sc0 sc1 nt
	v_lshl_add_u64 v[8:9], v[8:9], 0, s[44:45]
	global_load_dword v66, v[8:9], off sc0 sc1 nt
	v_lshl_add_u64 v[8:9], v[8:9], 0, s[44:45]
	global_load_dword v65, v[8:9], off sc0 sc1 nt
	v_lshl_add_u64 v[8:9], v[8:9], 0, s[44:45]
	global_load_dword v72, v[8:9], off sc0 sc1 nt
	v_lshl_add_u64 v[8:9], v[8:9], 0, s[44:45]
	global_load_dword v71, v[8:9], off sc0 sc1 nt
	v_lshl_add_u64 v[8:9], v[8:9], 0, s[44:45]
	global_load_dword v76, v[8:9], off sc0 sc1 nt
	v_lshl_add_u64 v[8:9], v[8:9], 0, s[44:45]
	global_load_dword v75, v[8:9], off sc0 sc1 nt
	v_lshl_add_u64 v[8:9], v[8:9], 0, s[44:45]
	global_load_dword v80, v[8:9], off sc0 sc1 nt
	v_lshl_add_u64 v[8:9], v[8:9], 0, s[44:45]
	global_load_dword v79, v[8:9], off sc0 sc1 nt
	v_lshl_add_u64 v[8:9], v[8:9], 0, s[44:45]
	global_load_dword v84, v[8:9], off sc0 sc1 nt
	v_lshl_add_u64 v[8:9], v[8:9], 0, s[44:45]
	global_load_dword v83, v[8:9], off sc0 sc1 nt
	v_lshl_add_u64 v[8:9], v[8:9], 0, s[44:45]
	global_load_dword v85, v[8:9], off sc0 sc1 nt
	v_lshl_add_u64 v[8:9], v[8:9], 0, s[44:45]
	global_load_dword v86, v[8:9], off sc0 sc1 nt
	v_lshl_add_u64 v[8:9], v[8:9], 0, s[44:45]
	global_load_dword v88, v[8:9], off sc0 sc1 nt
	v_lshl_add_u64 v[8:9], v[8:9], 0, s[44:45]
	global_load_dword v89, v[8:9], off sc0 sc1 nt
	v_lshl_add_u64 v[8:9], v[8:9], 0, s[44:45]
	global_load_dword v90, v[8:9], off sc0 sc1 nt
	v_lshl_add_u64 v[8:9], v[8:9], 0, s[44:45]
	global_load_dword v91, v[8:9], off sc0 sc1 nt
	v_lshl_add_u64 v[8:9], v[8:9], 0, s[44:45]
	global_load_dword v92, v[8:9], off sc0 sc1 nt
	global_load_dword v87, v[4:5], off sc0 sc1 nt
	v_mov_b32_e32 v5, 0
	v_mov_b32_e32 v3, v5
	v_lshlrev_b64 v[8:9], s42, v[2:3]
	v_and_b32_e32 v1, 7, v0
	v_lshl_add_u64 v[10:11], v[6:7], 0, v[8:9]
	v_lshlrev_b32_e32 v6, 2, v1
	v_lshl_add_u32 v4, v1, 11, s46
	v_bitop3_b32 v7, v2, v6, 8 bitop3:0x36
	v_xor_b32_e32 v1, v6, v2
	v_lshl_add_u32 v9, v7, 2, v4
	v_bitop3_b32 v7, v2, v6, 16 bitop3:0x36
	v_bitop3_b32 v6, v2, v6, 24 bitop3:0x36
	v_lshl_add_u32 v1, v1, 2, v4
	v_lshl_add_u32 v18, v7, 2, v4
	v_lshl_add_u32 v19, v6, 2, v4
	v_lshlrev_b32_e32 v4, 4, v0
	v_lshrrev_b32_e32 v20, 5, v170
	v_and_b32_e32 v6, 0x70, v4
	v_lshl_add_u32 v4, v20, 7, s46
	v_bitop3_b32 v8, v0, 4, 31 bitop3:0x6c
	s_add_u32 s73, s82, 0x24000000
	v_lshl_add_u32 v21, v8, 2, v4
	v_bitop3_b32 v8, v0, 8, 31 bitop3:0x6c
	s_addc_u32 s74, s83, 0
	v_lshl_add_u32 v22, v8, 2, v4
	v_bitop3_b32 v8, v0, 12, 31 bitop3:0x6c
	s_add_u32 s75, s82, 0x4000000
	v_lshl_add_u32 v23, v8, 2, v4
	v_bitop3_b32 v8, v0, 16, 31 bitop3:0x6c
	s_addc_u32 s76, s83, 0
	v_lshl_add_u32 v24, v8, 2, v4
	v_bitop3_b32 v8, v0, 20, 31 bitop3:0x6c
	s_add_u32 s77, s82, 0x2d000000
	v_lshl_add_u32 v25, v8, 2, v4
	v_bitop3_b32 v8, v0, 24, 31 bitop3:0x6c
	s_addc_u32 s78, s83, 0
	v_lshl_add_u32 v26, v8, 2, v4
	v_bitop3_b32 v8, v0, 28, 31 bitop3:0x6c
	s_add_u32 s79, s82, 0x30400000
	v_lshl_add_u32 v27, v8, 2, v4
	v_and_b32_e32 v8, 31, v0
	v_mov_b32_e32 v7, v5
	s_addc_u32 s88, s83, 0
	v_lshl_add_u32 v28, v8, 2, v4
	s_lshl_b32 s89, s33, 4
	s_mov_b32 s90, 0x2c00000
	s_mov_b32 s91, 0
	s_branch .LBB0_81

; #define MOE_LOAD(v, it) do { _Pragma("unroll") for (int i_ = 0; i_ < 64; ++i_) v[i_] = __builtin_nontemporal_load((it).src + (size_t)(2 * i_) * (it).stride); } while (0)
;     ...
;         for (int j = 0; j < nmine; j += 2) {
;             const int it1 = gw + (j + 1) * NGW, it2 = gw + (j + 2) * NGW;
;             ib = moe_item(wg, wu, wd, win, wout, wpn, wpd, F.ws, it1 <= last ? it1 : last, F.lane); MOE_LOAD(vb, ib);
;             MOE_PROC(va, ia);
;             ia = moe_item(wg, wu, wd, win, wout, wpn, wpd, F.ws, it2 <= last ? it2 : last, F.lane); MOE_LOAD(va, ia);
.LBB0_80:
	s_lshl_b64 s[68:69], s[68:69], 3
	v_lshl_add_u64 v[14:15], v[16:17], 0, s[68:69]
	global_load_dword v87, v[16:17], off sc0 sc1 nt
	v_lshl_add_u64 v[16:17], v[14:15], 0, s[68:69]
	v_lshl_add_u64 v[30:31], v[16:17], 0, s[68:69]
	v_lshl_add_u64 v[32:33], v[30:31], 0, s[68:69]
	v_lshl_add_u64 v[34:35], v[32:33], 0, s[68:69]
	v_lshl_add_u64 v[36:37], v[34:35], 0, s[68:69]
	v_lshl_add_u64 v[38:39], v[36:37], 0, s[68:69]
	v_lshl_add_u64 v[40:41], v[38:39], 0, s[68:69]
	global_load_dword v92, v[14:15], off sc0 sc1 nt
	global_load_dword v91, v[16:17], off sc0 sc1 nt
	global_load_dword v90, v[30:31], off sc0 sc1 nt
	global_load_dword v89, v[32:33], off sc0 sc1 nt
	global_load_dword v88, v[34:35], off sc0 sc1 nt
	global_load_dword v86, v[36:37], off sc0 sc1 nt
	global_load_dword v85, v[38:39], off sc0 sc1 nt
	global_load_dword v83, v[40:41], off sc0 sc1 nt
	v_lshl_add_u64 v[14:15], v[40:41], 0, s[68:69]
	v_lshl_add_u64 v[16:17], v[14:15], 0, s[68:69]
	global_load_dword v84, v[14:15], off sc0 sc1 nt
	global_load_dword v79, v[16:17], off sc0 sc1 nt
	v_lshl_add_u64 v[14:15], v[16:17], 0, s[68:69]
	global_load_dword v80, v[14:15], off sc0 sc1 nt
	v_lshl_add_u64 v[14:15], v[14:15], 0, s[68:69]
	global_load_dword v75, v[14:15], off sc0 sc1 nt
	v_lshl_add_u64 v[14:15], v[14:15], 0, s[68:69]
	global_load_dword v76, v[14:15], off sc0 sc1 nt
	v_lshl_add_u64 v[14:15], v[14:15], 0, s[68:69]
	global_load_dword v71, v[14:15], off sc0 sc1 nt
	v_lshl_add_u64 v[14:15], v[14:15], 0, s[68:69]
	global_load_dword v72, v[14:15], off sc0 sc1 nt
	v_lshl_add_u64 v[14:15], v[14:15], 0, s[68:69]
	global_load_dword v65, v[14:15], off sc0 sc1 nt
	v_lshl_add_u64 v[14:15], v[14:15], 0, s[68:69]
	global_load_dword v66, v[14:15], off sc0 sc1 nt
	v_lshl_add_u64 v[14:15], v[14:15], 0, s[68:69]
	global_load_dword v61, v[14:15], off sc0 sc1 nt
	v_lshl_add_u64 v[14:15], v[14:15], 0, s[68:69]
	global_load_dword v62, v[14:15], off sc0 sc1 nt
	v_lshl_add_u64 v[14:15], v[14:15], 0, s[68:69]
	global_load_dword v57, v[14:15], off sc0 sc1 nt
	v_lshl_add_u64 v[14:15], v[14:15], 0, s[68:69]
	global_load_dword v58, v[14:15], off sc0 sc1 nt
	v_lshl_add_u64 v[14:15], v[14:15], 0, s[68:69]
	global_load_dword v53, v[14:15], off sc0 sc1 nt
	v_lshl_add_u64 v[14:15], v[14:15], 0, s[68:69]
	global_load_dword v54, v[14:15], off sc0 sc1 nt
	v_lshl_add_u64 v[14:15], v[14:15], 0, s[68:69]
	global_load_dword v45, v[14:15], off sc0 sc1 nt
	v_lshl_add_u64 v[14:15], v[14:15], 0, s[68:69]
	global_load_dword v46, v[14:15], off sc0 sc1 nt
	v_lshl_add_u64 v[14:15], v[14:15], 0, s[68:69]
	global_load_dword v35, v[14:15], off sc0 sc1 nt
	v_lshl_add_u64 v[14:15], v[14:15], 0, s[68:69]
	global_load_dword v36, v[14:15], off sc0 sc1 nt
	v_lshl_add_u64 v[14:15], v[14:15], 0, s[68:69]
	global_load_dword v33, v[14:15], off sc0 sc1 nt
	v_lshl_add_u64 v[14:15], v[14:15], 0, s[68:69]
	global_load_dword v34, v[14:15], off sc0 sc1 nt
	v_lshl_add_u64 v[14:15], v[14:15], 0, s[68:69]
	global_load_dword v31, v[14:15], off sc0 sc1 nt
	v_lshl_add_u64 v[14:15], v[14:15], 0, s[68:69]
	global_load_dword v32, v[14:15], off sc0 sc1 nt
	v_lshl_add_u64 v[14:15], v[14:15], 0, s[68:69]
	global_load_dword v29, v[14:15], off sc0 sc1 nt
	v_lshl_add_u64 v[14:15], v[14:15], 0, s[68:69]
	global_load_dword v30, v[14:15], off sc0 sc1 nt
	v_lshl_add_u64 v[14:15], v[14:15], 0, s[68:69]
	global_load_dword v81, v[14:15], off sc0 sc1 nt
	v_lshl_add_u64 v[14:15], v[14:15], 0, s[68:69]
	global_load_dword v82, v[14:15], off sc0 sc1 nt
	v_lshl_add_u64 v[14:15], v[14:15], 0, s[68:69]
	global_load_dword v77, v[14:15], off sc0 sc1 nt
	v_lshl_add_u64 v[14:15], v[14:15], 0, s[68:69]
	global_load_dword v78, v[14:15], off sc0 sc1 nt
	v_lshl_add_u64 v[14:15], v[14:15], 0, s[68:69]
	global_load_dword v73, v[14:15], off sc0 sc1 nt
	v_lshl_add_u64 v[14:15], v[14:15], 0, s[68:69]
	global_load_dword v74, v[14:15], off sc0 sc1 nt
	v_lshl_add_u64 v[14:15], v[14:15], 0, s[68:69]
	global_load_dword v69, v[14:15], off sc0 sc1 nt
	v_lshl_add_u64 v[14:15], v[14:15], 0, s[68:69]
	global_load_dword v70, v[14:15], off sc0 sc1 nt
	v_lshl_add_u64 v[14:15], v[14:15], 0, s[68:69]
	global_load_dword v67, v[14:15], off sc0 sc1 nt
	v_lshl_add_u64 v[14:15], v[14:15], 0, s[68:69]
	global_load_dword v68, v[14:15], off sc0 sc1 nt
	v_lshl_add_u64 v[14:15], v[14:15], 0, s[68:69]
	global_load_dword v63, v[14:15], off sc0 sc1 nt
	v_lshl_add_u64 v[14:15], v[14:15], 0, s[68:69]
	global_load_dword v64, v[14:15], off sc0 sc1 nt
	v_lshl_add_u64 v[14:15], v[14:15], 0, s[68:69]
	global_load_dword v59, v[14:15], off sc0 sc1 nt
	v_lshl_add_u64 v[14:15], v[14:15], 0, s[68:69]
	global_load_dword v60, v[14:15], off sc0 sc1 nt
	v_lshl_add_u64 v[14:15], v[14:15], 0, s[68:69]
	global_load_dword v55, v[14:15], off sc0 sc1 nt
	v_lshl_add_u64 v[14:15], v[14:15], 0, s[68:69]
	global_load_dword v56, v[14:15], off sc0 sc1 nt
	v_lshl_add_u64 v[14:15], v[14:15], 0, s[68:69]
	global_load_dword v51, v[14:15], off sc0 sc1 nt
	v_lshl_add_u64 v[14:15], v[14:15], 0, s[68:69]
	global_load_dword v52, v[14:15], off sc0 sc1 nt
	v_lshl_add_u64 v[14:15], v[14:15], 0, s[68:69]
	global_load_dword v38, v[14:15], off sc0 sc1 nt
	v_lshl_add_u64 v[14:15], v[14:15], 0, s[68:69]
	global_load_dword v39, v[14:15], off sc0 sc1 nt
	v_lshl_add_u64 v[14:15], v[14:15], 0, s[68:69]
	global_load_dword v40, v[14:15], off sc0 sc1 nt
	v_lshl_add_u64 v[14:15], v[14:15], 0, s[68:69]
	global_load_dword v42, v[14:15], off sc0 sc1 nt
	v_lshl_add_u64 v[14:15], v[14:15], 0, s[68:69]
	global_load_dword v37, v[14:15], off sc0 sc1 nt
	v_lshl_add_u64 v[14:15], v[14:15], 0, s[68:69]
	global_load_dword v41, v[14:15], off sc0 sc1 nt
	v_lshl_add_u64 v[14:15], v[14:15], 0, s[68:69]
	global_load_dword v43, v[14:15], off sc0 sc1 nt
	v_lshl_add_u64 v[14:15], v[14:15], 0, s[68:69]
	global_load_dword v44, v[14:15], off sc0 sc1 nt
	v_lshl_add_u64 v[14:15], v[14:15], 0, s[68:69]
	global_load_dword v47, v[14:15], off sc0 sc1 nt
	v_lshl_add_u64 v[14:15], v[14:15], 0, s[68:69]
	global_load_dword v48, v[14:15], off sc0 sc1 nt
	v_lshl_add_u64 v[14:15], v[14:15], 0, s[68:69]
	global_load_dword v49, v[14:15], off sc0 sc1 nt
	v_lshl_add_u64 v[14:15], v[14:15], 0, s[68:69]
	s_waitcnt vmcnt(62)
;     ...
;             MOE_PROC(vb, ib);
	ds_write2st64_b32 v28, v93, v101 offset1:1
	ds_write2st64_b32 v28, v99, v100 offset0:2 offset1:3
	ds_write2st64_b32 v28, v97, v98 offset0:4 offset1:5
	ds_write2st64_b32 v28, v95, v96 offset0:6 offset1:7
	ds_write2st64_b32 v21, v94, v124 offset0:8 offset1:9
	ds_write2st64_b32 v21, v104, v114 offset0:10 offset1:11
	ds_write2st64_b32 v21, v105, v115 offset0:12 offset1:13
	ds_write2st64_b32 v21, v106, v116 offset0:14 offset1:15
	ds_write2st64_b32 v22, v107, v117 offset0:16 offset1:17
	ds_write2st64_b32 v22, v108, v118 offset0:18 offset1:19
	ds_write2st64_b32 v22, v109, v119 offset0:20 offset1:21
	ds_write2st64_b32 v22, v110, v120 offset0:22 offset1:23
	ds_write2st64_b32 v23, v111, v121 offset0:24 offset1:25
	ds_write2st64_b32 v23, v112, v122 offset0:26 offset1:27
	global_load_dword v50, v[14:15], off sc0 sc1 nt
	ds_write2st64_b32 v23, v102, v103 offset0:28 offset1:29
	ds_write2st64_b32 v23, v113, v123 offset0:30 offset1:31
	ds_write2st64_b32 v24, v125, v126 offset0:32 offset1:33
	ds_write2st64_b32 v24, v127, v128 offset0:34 offset1:35
	ds_write2st64_b32 v24, v129, v130 offset0:36 offset1:37
	ds_write2st64_b32 v24, v131, v132 offset0:38 offset1:39
	ds_write2st64_b32 v25, v133, v134 offset0:40 offset1:41
	ds_write2st64_b32 v25, v135, v136 offset0:42 offset1:43
	ds_write2st64_b32 v25, v137, v138 offset0:44 offset1:45
	ds_write2st64_b32 v25, v139, v140 offset0:46 offset1:47
	ds_write2st64_b32 v26, v141, v142 offset0:48 offset1:49
	ds_write2st64_b32 v26, v143, v144 offset0:50 offset1:51
	ds_write2st64_b32 v26, v146, v147 offset0:52 offset1:53
	ds_write2st64_b32 v26, v148, v149 offset0:54 offset1:55
	ds_write2st64_b32 v27, v151, v152 offset0:56 offset1:57
	ds_write2st64_b32 v27, v153, v154 offset0:58 offset1:59
	ds_write2st64_b32 v27, v155, v157 offset0:60 offset1:61
	ds_write2st64_b32 v27, v158, v159 offset0:62 offset1:63
	s_waitcnt lgkmcnt(0)
	ds_read2_b32 v[16:17], v1 offset1:32
	v_lshlrev_b64 v[14:15], s44, v[2:3]
	v_lshl_add_u64 v[12:13], v[12:13], 0, v[14:15]
	v_lshl_add_u64 v[98:99], v[12:13], 0, v[6:7]
	v_mov_b32_e32 v12, 0
	s_waitcnt lgkmcnt(0)
	v_mul_f32_e32 v4, 0x42800000, v16
	v_mul_f32_e32 v13, 0x42800000, v17
	ds_read2_b32 v[16:17], v1 offset0:64 offset1:96
	ds_read2_b32 v[94:95], v1 offset0:128 offset1:160
	v_cvt_pk_fp8_f32 v12, v4, v13
	v_lshlrev_b64 v[14:15], s46, v[2:3]
	v_lshl_add_u64 v[10:11], v[10:11], 0, v[14:15]
	s_waitcnt lgkmcnt(1)
	v_mul_f32_e32 v4, 0x42800000, v16
	v_mul_f32_e32 v13, 0x42800000, v17
	v_cvt_pk_fp8_f32 v12, v4, v13 op_sel:[0,0,1]
	s_waitcnt lgkmcnt(0)
	v_mul_f32_e32 v4, 0x42800000, v94
	ds_read2_b32 v[14:15], v1 offset0:192 offset1:224
	v_mul_f32_e32 v16, 0x42800000, v95
	v_mov_b32_e32 v13, 0
	v_cvt_pk_fp8_f32 v13, v4, v16
	ds_read2_b32 v[16:17], v145 offset1:32
	s_waitcnt lgkmcnt(1)
	v_mul_f32_e32 v4, 0x42800000, v14
	v_mul_f32_e32 v93, 0x42800000, v15
	ds_read2_b32 v[14:15], v145 offset0:64 offset1:96
	v_cvt_pk_fp8_f32 v13, v4, v93 op_sel:[0,0,1]
	s_waitcnt lgkmcnt(1)
	v_mul_f32_e32 v4, 0x42800000, v16
	v_mul_f32_e32 v93, 0x42800000, v17
	ds_read2_b32 v[16:17], v145 offset0:128 offset1:160
	s_waitcnt lgkmcnt(1)
	v_mul_f32_e32 v96, 0x42800000, v14
	v_mov_b32_e32 v14, 0
	v_cvt_pk_fp8_f32 v14, v4, v93
	v_mul_f32_e32 v97, 0x42800000, v15
	s_waitcnt lgkmcnt(0)
	v_mul_f32_e32 v4, 0x42800000, v16
	v_mul_f32_e32 v93, 0x42800000, v17
	ds_read2_b32 v[16:17], v145 offset0:192 offset1:224
	v_mov_b32_e32 v15, 0
	v_cvt_pk_fp8_f32 v15, v4, v93
	ds_read2_b32 v[94:95], v9 offset1:32
	v_cvt_pk_fp8_f32 v14, v96, v97 op_sel:[0,0,1]
	s_waitcnt lgkmcnt(1)
	v_mul_f32_e32 v4, 0x42800000, v16
	v_mul_f32_e32 v16, 0x42800000, v17
	v_cvt_pk_fp8_f32 v15, v4, v16 op_sel:[0,0,1]
	ds_read2_b32 v[16:17], v9 offset0:64 offset1:96
	s_waitcnt lgkmcnt(1)
	v_mul_f32_e32 v4, 0x42800000, v94
	v_mul_f32_e32 v93, 0x42800000, v95
	v_mov_b32_e32 v94, 0
	ds_read2_b32 v[96:97], v9 offset0:128 offset1:160
	v_cvt_pk_fp8_f32 v94, v4, v93
	global_store_dwordx4 v[98:99], v[12:15], off sc0 sc1 nt
	s_waitcnt lgkmcnt(1)
	v_mul_f32_e32 v4, 0x42800000, v16
	v_mov_b32_e32 v95, 0
	v_mul_f32_e32 v12, 0x42800000, v17
	v_cvt_pk_fp8_f32 v94, v4, v12 op_sel:[0,0,1]
	s_waitcnt lgkmcnt(0)
	v_mul_f32_e32 v4, 0x42800000, v96
	ds_read2_b32 v[12:13], v9 offset0:192 offset1:224
	v_mul_f32_e32 v14, 0x42800000, v97
	v_cvt_pk_fp8_f32 v95, v4, v14
	ds_read2_b32 v[14:15], v150 offset1:32
	v_mov_b32_e32 v96, 0
	s_waitcnt lgkmcnt(1)
; #define MOE_LOAD(v, it) do { _Pragma("unroll") for (int i_ = 0; i_ < 64; ++i_) v[i_] = __builtin_nontemporal_load((it).src + (size_t)(2 * i_) * (it).stride); } while (0)
;     ...
;         for (int j = 0; j < nmine; j += 2) {
;             const int it1 = gw + (j + 1) * NGW, it2 = gw + (j + 2) * NGW;
;             ib = moe_item(wg, wu, wd, win, wout, wpn, wpd, F.ws, it1 <= last ? it1 : last, F.lane); MOE_LOAD(vb, ib);
;             MOE_PROC(va, ia);
;             ia = moe_item(wg, wu, wd, win, wout, wpn, wpd, F.ws, it2 <= last ? it2 : last, F.lane); MOE_LOAD(va, ia);
;             MOE_PROC(vb, ib);
;         }
	v_mul_f32_e32 v4, 0x42800000, v12
	v_mul_f32_e32 v16, 0x42800000, v13
	ds_read2_b32 v[12:13], v150 offset0:64 offset1:96
	v_cvt_pk_fp8_f32 v95, v4, v16 op_sel:[0,0,1]
	s_waitcnt lgkmcnt(1)
	v_mul_f32_e32 v4, 0x42800000, v14
	v_mul_f32_e32 v16, 0x42800000, v15
	ds_read2_b32 v[14:15], v150 offset0:128 offset1:160
	s_waitcnt lgkmcnt(1)
	v_mul_f32_e32 v17, 0x42800000, v12
	v_mul_f32_e32 v93, 0x42800000, v13
	ds_read2_b32 v[12:13], v150 offset0:192 offset1:224
	v_cvt_pk_fp8_f32 v96, v4, v16
	s_waitcnt lgkmcnt(1)
	v_mul_f32_e32 v4, 0x42800000, v14
	v_mul_f32_e32 v14, 0x42800000, v15
	v_mov_b32_e32 v97, 0
	v_cvt_pk_fp8_f32 v97, v4, v14
	s_waitcnt lgkmcnt(0)
	v_mul_f32_e32 v4, 0x42800000, v12
	v_mul_f32_e32 v12, 0x42800000, v13
	v_cvt_pk_fp8_f32 v96, v17, v93 op_sel:[0,0,1]
	v_cvt_pk_fp8_f32 v97, v4, v12 op_sel:[0,0,1]
	s_lshl_b32 s4, s42, 3
	ds_read2_b32 v[12:13], v18 offset1:32
	v_lshl_add_u64 v[16:17], v[98:99], 0, s[4:5]
	ds_read2_b32 v[14:15], v18 offset0:64 offset1:96
	global_store_dwordx4 v[16:17], v[94:97], off sc0 sc1 nt
	ds_read2_b32 v[94:95], v18 offset0:128 offset1:160
	s_waitcnt lgkmcnt(2)
	v_mul_f32_e32 v4, 0x42800000, v12
	v_mul_f32_e32 v13, 0x42800000, v13
	v_mov_b32_e32 v12, 0
	s_waitcnt lgkmcnt(1)
	v_mul_f32_e32 v93, 0x42800000, v14
	v_mul_f32_e32 v96, 0x42800000, v15
	v_cvt_pk_fp8_f32 v12, v4, v13
	s_waitcnt lgkmcnt(0)
	v_mul_f32_e32 v4, 0x42800000, v94
	v_mul_f32_e32 v94, 0x42800000, v95
	ds_read2_b32 v[14:15], v18 offset0:192 offset1:224
	v_mov_b32_e32 v13, 0
	v_cvt_pk_fp8_f32 v13, v4, v94
	ds_read2_b32 v[94:95], v156 offset1:32
	v_cvt_pk_fp8_f32 v12, v93, v96 op_sel:[0,0,1]
	s_waitcnt lgkmcnt(1)
	v_mul_f32_e32 v4, 0x42800000, v14
	v_mul_f32_e32 v14, 0x42800000, v15
	ds_read2_b32 v[96:97], v156 offset0:64 offset1:96
	v_cvt_pk_fp8_f32 v13, v4, v14 op_sel:[0,0,1]
	s_waitcnt lgkmcnt(1)
	v_mul_f32_e32 v4, 0x42800000, v94
	v_mul_f32_e32 v15, 0x42800000, v95
	v_mov_b32_e32 v14, 0
	ds_read2_b32 v[94:95], v156 offset0:128 offset1:160
	v_cvt_pk_fp8_f32 v14, v4, v15
	s_waitcnt lgkmcnt(1)
	v_mul_f32_e32 v4, 0x42800000, v96
	v_mul_f32_e32 v15, 0x42800000, v97
	ds_read2_b32 v[96:97], v156 offset0:192 offset1:224
	v_cvt_pk_fp8_f32 v14, v4, v15 op_sel:[0,0,1]
	s_waitcnt lgkmcnt(1)
	v_mul_f32_e32 v4, 0x42800000, v94
	v_mul_f32_e32 v93, 0x42800000, v95
	ds_read2_b32 v[94:95], v19 offset1:32
	s_waitcnt lgkmcnt(1)
	v_mul_f32_e32 v100, 0x42800000, v96
	v_mul_f32_e32 v101, 0x42800000, v97
	v_mov_b32_e32 v15, 0
	ds_read2_b32 v[96:97], v19 offset0:64 offset1:96
	v_cvt_pk_fp8_f32 v15, v4, v93
	s_waitcnt lgkmcnt(1)
	v_mul_f32_e32 v4, 0x42800000, v94
	v_mul_f32_e32 v93, 0x42800000, v95
	v_mov_b32_e32 v94, 0
	ds_read2_b32 v[98:99], v19 offset0:128 offset1:160
	v_cvt_pk_fp8_f32 v94, v4, v93
	s_waitcnt lgkmcnt(1)
	v_mul_f32_e32 v4, 0x42800000, v96
	v_mul_f32_e32 v93, 0x42800000, v97
	ds_read2_b32 v[96:97], v19 offset0:192 offset1:224
	v_cvt_pk_fp8_f32 v94, v4, v93 op_sel:[0,0,1]
	s_waitcnt lgkmcnt(1)
	v_mul_f32_e32 v4, 0x42800000, v98
	v_mul_f32_e32 v93, 0x42800000, v99
	v_mov_b32_e32 v95, 0
	ds_read2_b32 v[98:99], v160 offset1:32
	v_cvt_pk_fp8_f32 v95, v4, v93
	s_waitcnt lgkmcnt(1)
	v_mul_f32_e32 v4, 0x42800000, v96
	v_mul_f32_e32 v93, 0x42800000, v97
	ds_read2_b32 v[96:97], v160 offset0:64 offset1:96
	v_cvt_pk_fp8_f32 v95, v4, v93 op_sel:[0,0,1]
	s_waitcnt lgkmcnt(1)
	v_mul_f32_e32 v4, 0x42800000, v98
	v_mul_f32_e32 v93, 0x42800000, v99
	ds_read2_b32 v[98:99], v160 offset0:128 offset1:160
	v_cvt_pk_fp8_f32 v15, v100, v101 op_sel:[0,0,1]
	s_waitcnt lgkmcnt(1)
	v_mul_f32_e32 v102, 0x42800000, v96
	v_mov_b32_e32 v96, 0
	ds_read2_b32 v[100:101], v160 offset0:192 offset1:224
	v_mul_f32_e32 v103, 0x42800000, v97
	v_cvt_pk_fp8_f32 v96, v4, v93
	s_waitcnt lgkmcnt(1)
	v_mul_f32_e32 v4, 0x42800000, v98
	v_mul_f32_e32 v93, 0x42800000, v99
	v_mov_b32_e32 v97, 0
	v_cvt_pk_fp8_f32 v97, v4, v93
	s_waitcnt lgkmcnt(0)
	v_mul_f32_e32 v4, 0x42800000, v100
	v_mul_f32_e32 v93, 0x42800000, v101
	v_cvt_pk_fp8_f32 v96, v102, v103 op_sel:[0,0,1]
	v_cvt_pk_fp8_f32 v97, v4, v93 op_sel:[0,0,1]
	v_lshl_add_u64 v[16:17], v[16:17], 0, s[4:5]
	global_store_dwordx4 v[16:17], v[12:15], off sc0 sc1 nt
	s_add_i32 s91, s91, 2
	s_cmp_ge_i32 s91, s6
	v_lshl_add_u64 v[12:13], v[16:17], 0, s[4:5]
	global_store_dwordx4 v[12:13], v[94:97], off sc0 sc1 nt
	s_waitcnt lgkmcnt(0)
	s_cbranch_scc1 .LBB0_130

; #define MOE_LOAD(v, it) do { _Pragma("unroll") for (int i_ = 0; i_ < 64; ++i_) v[i_] = __builtin_nontemporal_load((it).src + (size_t)(2 * i_) * (it).stride); } while (0)
;     ...
;             ib = moe_item(wg, wu, wd, win, wout, wpn, wpd, F.ws, it1 <= last ? it1 : last, F.lane); MOE_LOAD(vb, ib);
;             MOE_PROC(va, ia);
.LBB0_105:
	s_lshl_b64 s[46:47], s[46:47], 3
	global_load_dword v93, v[16:17], off sc0 sc1 nt
	v_lshl_add_u64 v[16:17], v[16:17], 0, s[46:47]
	v_lshl_add_u64 v[94:95], v[16:17], 0, s[46:47]
	v_lshl_add_u64 v[96:97], v[94:95], 0, s[46:47]
	v_lshl_add_u64 v[102:103], v[96:97], 0, s[46:47]
	v_lshl_add_u64 v[104:105], v[102:103], 0, s[46:47]
	v_lshl_add_u64 v[106:107], v[104:105], 0, s[46:47]
	v_lshl_add_u64 v[108:109], v[106:107], 0, s[46:47]
	v_lshl_add_u64 v[110:111], v[108:109], 0, s[46:47]
	global_load_dword v101, v[16:17], off sc0 sc1 nt
	global_load_dword v99, v[94:95], off sc0 sc1 nt
	global_load_dword v100, v[96:97], off sc0 sc1 nt
	s_nop 0
	global_load_dword v97, v[102:103], off sc0 sc1 nt
	global_load_dword v98, v[104:105], off sc0 sc1 nt
	global_load_dword v95, v[106:107], off sc0 sc1 nt
	global_load_dword v96, v[108:109], off sc0 sc1 nt
	global_load_dword v94, v[110:111], off sc0 sc1 nt
	v_lshl_add_u64 v[16:17], v[110:111], 0, s[46:47]
	s_waitcnt vmcnt(9)
	ds_write2st64_b32 v28, v87, v92 offset1:1
	v_lshl_add_u64 v[102:103], v[16:17], 0, s[46:47]
	global_load_dword v124, v[16:17], off sc0 sc1 nt
	global_load_dword v104, v[102:103], off sc0 sc1 nt
	v_lshl_add_u64 v[16:17], v[102:103], 0, s[46:47]
	global_load_dword v114, v[16:17], off sc0 sc1 nt
	v_lshl_add_u64 v[16:17], v[16:17], 0, s[46:47]
	global_load_dword v105, v[16:17], off sc0 sc1 nt
	v_lshl_add_u64 v[16:17], v[16:17], 0, s[46:47]
	global_load_dword v115, v[16:17], off sc0 sc1 nt
	v_lshl_add_u64 v[16:17], v[16:17], 0, s[46:47]
	global_load_dword v106, v[16:17], off sc0 sc1 nt
	v_lshl_add_u64 v[16:17], v[16:17], 0, s[46:47]
	global_load_dword v116, v[16:17], off sc0 sc1 nt
	v_lshl_add_u64 v[16:17], v[16:17], 0, s[46:47]
	global_load_dword v107, v[16:17], off sc0 sc1 nt
	v_lshl_add_u64 v[16:17], v[16:17], 0, s[46:47]
	global_load_dword v117, v[16:17], off sc0 sc1 nt
	v_lshl_add_u64 v[16:17], v[16:17], 0, s[46:47]
	global_load_dword v108, v[16:17], off sc0 sc1 nt
	v_lshl_add_u64 v[16:17], v[16:17], 0, s[46:47]
	global_load_dword v118, v[16:17], off sc0 sc1 nt
	v_lshl_add_u64 v[16:17], v[16:17], 0, s[46:47]
	global_load_dword v109, v[16:17], off sc0 sc1 nt
	v_lshl_add_u64 v[16:17], v[16:17], 0, s[46:47]
	global_load_dword v119, v[16:17], off sc0 sc1 nt
	v_lshl_add_u64 v[16:17], v[16:17], 0, s[46:47]
	global_load_dword v110, v[16:17], off sc0 sc1 nt
	v_lshl_add_u64 v[16:17], v[16:17], 0, s[46:47]
	global_load_dword v120, v[16:17], off sc0 sc1 nt
	v_lshl_add_u64 v[16:17], v[16:17], 0, s[46:47]
	global_load_dword v111, v[16:17], off sc0 sc1 nt
	v_lshl_add_u64 v[16:17], v[16:17], 0, s[46:47]
	global_load_dword v121, v[16:17], off sc0 sc1 nt
	v_lshl_add_u64 v[16:17], v[16:17], 0, s[46:47]
	global_load_dword v112, v[16:17], off sc0 sc1 nt
	v_lshl_add_u64 v[16:17], v[16:17], 0, s[46:47]
	global_load_dword v122, v[16:17], off sc0 sc1 nt
	v_lshl_add_u64 v[16:17], v[16:17], 0, s[46:47]
	global_load_dword v102, v[16:17], off sc0 sc1 nt
	v_lshl_add_u64 v[16:17], v[16:17], 0, s[46:47]
	global_load_dword v103, v[16:17], off sc0 sc1 nt
	v_lshl_add_u64 v[16:17], v[16:17], 0, s[46:47]
	global_load_dword v113, v[16:17], off sc0 sc1 nt
	v_lshl_add_u64 v[16:17], v[16:17], 0, s[46:47]
	global_load_dword v123, v[16:17], off sc0 sc1 nt
	v_lshl_add_u64 v[16:17], v[16:17], 0, s[46:47]
	global_load_dword v125, v[16:17], off sc0 sc1 nt
	v_lshl_add_u64 v[16:17], v[16:17], 0, s[46:47]
	global_load_dword v126, v[16:17], off sc0 sc1 nt
	v_lshl_add_u64 v[16:17], v[16:17], 0, s[46:47]
	global_load_dword v127, v[16:17], off sc0 sc1 nt
	v_lshl_add_u64 v[16:17], v[16:17], 0, s[46:47]
	global_load_dword v128, v[16:17], off sc0 sc1 nt
	v_lshl_add_u64 v[16:17], v[16:17], 0, s[46:47]
	global_load_dword v129, v[16:17], off sc0 sc1 nt
	v_lshl_add_u64 v[16:17], v[16:17], 0, s[46:47]
	global_load_dword v130, v[16:17], off sc0 sc1 nt
	v_lshl_add_u64 v[16:17], v[16:17], 0, s[46:47]
	global_load_dword v131, v[16:17], off sc0 sc1 nt
	v_lshl_add_u64 v[16:17], v[16:17], 0, s[46:47]
	global_load_dword v132, v[16:17], off sc0 sc1 nt
	v_lshl_add_u64 v[16:17], v[16:17], 0, s[46:47]
	global_load_dword v133, v[16:17], off sc0 sc1 nt
	v_lshl_add_u64 v[16:17], v[16:17], 0, s[46:47]
	global_load_dword v134, v[16:17], off sc0 sc1 nt
	v_lshl_add_u64 v[16:17], v[16:17], 0, s[46:47]
	global_load_dword v135, v[16:17], off sc0 sc1 nt
	v_lshl_add_u64 v[16:17], v[16:17], 0, s[46:47]
	global_load_dword v136, v[16:17], off sc0 sc1 nt
	v_lshl_add_u64 v[16:17], v[16:17], 0, s[46:47]
	global_load_dword v137, v[16:17], off sc0 sc1 nt
	v_lshl_add_u64 v[16:17], v[16:17], 0, s[46:47]
	global_load_dword v138, v[16:17], off sc0 sc1 nt
	v_lshl_add_u64 v[16:17], v[16:17], 0, s[46:47]
	global_load_dword v139, v[16:17], off sc0 sc1 nt
	v_lshl_add_u64 v[16:17], v[16:17], 0, s[46:47]
	global_load_dword v140, v[16:17], off sc0 sc1 nt
	v_lshl_add_u64 v[16:17], v[16:17], 0, s[46:47]
	global_load_dword v141, v[16:17], off sc0 sc1 nt
	v_lshl_add_u64 v[16:17], v[16:17], 0, s[46:47]
	global_load_dword v142, v[16:17], off sc0 sc1 nt
	v_lshl_add_u64 v[16:17], v[16:17], 0, s[46:47]
	global_load_dword v143, v[16:17], off sc0 sc1 nt
	v_lshl_add_u64 v[16:17], v[16:17], 0, s[46:47]
	global_load_dword v144, v[16:17], off sc0 sc1 nt
	v_lshl_add_u64 v[16:17], v[16:17], 0, s[46:47]
	global_load_dword v146, v[16:17], off sc0 sc1 nt
	v_lshl_add_u64 v[16:17], v[16:17], 0, s[46:47]
	global_load_dword v147, v[16:17], off sc0 sc1 nt
	v_lshl_add_u64 v[16:17], v[16:17], 0, s[46:47]
	global_load_dword v148, v[16:17], off sc0 sc1 nt
	v_lshl_add_u64 v[16:17], v[16:17], 0, s[46:47]
	global_load_dword v149, v[16:17], off sc0 sc1 nt
	v_lshl_add_u64 v[16:17], v[16:17], 0, s[46:47]
;     ...
;             MOE_PROC(va, ia);
	global_load_dword v151, v[16:17], off sc0 sc1 nt
	v_lshl_add_u64 v[16:17], v[16:17], 0, s[46:47]
	global_load_dword v152, v[16:17], off sc0 sc1 nt
	v_lshl_add_u64 v[16:17], v[16:17], 0, s[46:47]
	global_load_dword v153, v[16:17], off sc0 sc1 nt
	v_lshl_add_u64 v[16:17], v[16:17], 0, s[46:47]
	global_load_dword v154, v[16:17], off sc0 sc1 nt
	v_lshl_add_u64 v[16:17], v[16:17], 0, s[46:47]
	global_load_dword v155, v[16:17], off sc0 sc1 nt
	v_lshl_add_u64 v[16:17], v[16:17], 0, s[46:47]
	global_load_dword v157, v[16:17], off sc0 sc1 nt
	v_lshl_add_u64 v[16:17], v[16:17], 0, s[46:47]
	global_load_dword v158, v[16:17], off sc0 sc1 nt
	v_lshl_add_u64 v[16:17], v[16:17], 0, s[46:47]
	ds_write2st64_b32 v28, v91, v90 offset0:2 offset1:3
	ds_write2st64_b32 v28, v89, v88 offset0:4 offset1:5
	ds_write2st64_b32 v28, v86, v85 offset0:6 offset1:7
	ds_write2st64_b32 v21, v83, v84 offset0:8 offset1:9
	ds_write2st64_b32 v21, v79, v80 offset0:10 offset1:11
	ds_write2st64_b32 v21, v75, v76 offset0:12 offset1:13
	ds_write2st64_b32 v21, v71, v72 offset0:14 offset1:15
	ds_write2st64_b32 v22, v65, v66 offset0:16 offset1:17
	ds_write2st64_b32 v22, v61, v62 offset0:18 offset1:19
	ds_write2st64_b32 v22, v57, v58 offset0:20 offset1:21
	ds_write2st64_b32 v22, v53, v54 offset0:22 offset1:23
	ds_write2st64_b32 v23, v45, v46 offset0:24 offset1:25
	ds_write2st64_b32 v23, v35, v36 offset0:26 offset1:27
	ds_write2st64_b32 v23, v33, v34 offset0:28 offset1:29
	ds_write2st64_b32 v23, v31, v32 offset0:30 offset1:31
	ds_write2st64_b32 v24, v29, v30 offset0:32 offset1:33
	ds_write2st64_b32 v24, v81, v82 offset0:34 offset1:35
	ds_write2st64_b32 v24, v77, v78 offset0:36 offset1:37
	ds_write2st64_b32 v24, v73, v74 offset0:38 offset1:39
	ds_write2st64_b32 v25, v69, v70 offset0:40 offset1:41
	ds_write2st64_b32 v25, v67, v68 offset0:42 offset1:43
	ds_write2st64_b32 v25, v63, v64 offset0:44 offset1:45
	ds_write2st64_b32 v25, v59, v60 offset0:46 offset1:47
	ds_write2st64_b32 v26, v55, v56 offset0:48 offset1:49
	ds_write2st64_b32 v26, v51, v52 offset0:50 offset1:51
	global_load_dword v159, v[16:17], off sc0 sc1 nt
	ds_write2st64_b32 v26, v38, v39 offset0:52 offset1:53
	ds_write2st64_b32 v26, v40, v42 offset0:54 offset1:55
	ds_write2st64_b32 v27, v37, v41 offset0:56 offset1:57
	ds_write2st64_b32 v27, v43, v44 offset0:58 offset1:59
	ds_write2st64_b32 v27, v47, v48 offset0:60 offset1:61
	ds_write2st64_b32 v27, v49, v50 offset0:62 offset1:63
	s_waitcnt lgkmcnt(0)
	ds_read2_b32 v[16:17], v1 offset1:32
	v_mov_b32_e32 v30, 0
	ds_read2_b32 v[32:33], v1 offset0:128 offset1:160
	v_mov_b32_e32 v31, 0
	v_add_u32_e32 v145, 0x400, v1
	s_waitcnt lgkmcnt(1)
	v_mul_f32_e32 v4, 0x42800000, v16
	v_mul_f32_e32 v15, 0x42800000, v17
	ds_read2_b32 v[16:17], v1 offset0:64 offset1:96
	v_cvt_pk_fp8_f32 v30, v4, v15
	ds_read2_b32 v[34:35], v145 offset0:128 offset1:160
	v_add_u32_e32 v150, 0x400, v9
	ds_read2_b32 v[38:39], v150 offset0:128 offset1:160
	s_waitcnt lgkmcnt(2)
	v_mul_f32_e32 v4, 0x42800000, v16
	v_mul_f32_e32 v15, 0x42800000, v17
	ds_read2_b32 v[16:17], v1 offset0:192 offset1:224
	v_cvt_pk_fp8_f32 v30, v4, v15 op_sel:[0,0,1]
	v_mul_f32_e32 v4, 0x42800000, v32
	v_mul_f32_e32 v15, 0x42800000, v33
	v_cvt_pk_fp8_f32 v31, v4, v15
	s_waitcnt lgkmcnt(0)
	v_mul_f32_e32 v4, 0x42800000, v16
	v_mul_f32_e32 v15, 0x42800000, v17
	ds_read2_b32 v[16:17], v145 offset0:64 offset1:96
	ds_read2_b32 v[32:33], v145 offset1:32
	v_cvt_pk_fp8_f32 v31, v4, v15 op_sel:[0,0,1]
	v_lshl_add_u64 v[10:11], v[10:11], 0, v[6:7]
	v_add_u32_e32 v156, 0x400, v18
	s_waitcnt lgkmcnt(1)
	v_mul_f32_e32 v29, 0x42800000, v16
	v_mul_f32_e32 v36, 0x42800000, v17
	ds_read2_b32 v[16:17], v145 offset0:192 offset1:224
	s_waitcnt lgkmcnt(1)
	v_mul_f32_e32 v4, 0x42800000, v32
	v_mul_f32_e32 v15, 0x42800000, v33
	v_mov_b32_e32 v32, 0
	v_cvt_pk_fp8_f32 v32, v4, v15
	v_mul_f32_e32 v4, 0x42800000, v34
	v_mul_f32_e32 v15, 0x42800000, v35
	v_mov_b32_e32 v33, 0
	ds_read2_b32 v[34:35], v9 offset1:32
	v_cvt_pk_fp8_f32 v33, v4, v15
	s_waitcnt lgkmcnt(1)
	v_mul_f32_e32 v4, 0x42800000, v16
	v_mul_f32_e32 v15, 0x42800000, v17
	ds_read2_b32 v[16:17], v9 offset0:64 offset1:96
	v_cvt_pk_fp8_f32 v32, v29, v36 op_sel:[0,0,1]
	ds_read2_b32 v[36:37], v9 offset0:128 offset1:160
	v_cvt_pk_fp8_f32 v33, v4, v15 op_sel:[0,0,1]
	s_waitcnt lgkmcnt(2)
	v_mul_f32_e32 v4, 0x42800000, v34
	v_mul_f32_e32 v15, 0x42800000, v35
	v_mov_b32_e32 v34, 0
	v_cvt_pk_fp8_f32 v34, v4, v15
	s_waitcnt lgkmcnt(1)
	v_mul_f32_e32 v4, 0x42800000, v16
	v_mul_f32_e32 v15, 0x42800000, v17
	ds_read2_b32 v[16:17], v9 offset0:192 offset1:224
	s_waitcnt lgkmcnt(1)
	v_mul_f32_e32 v29, 0x42800000, v36
	v_mul_f32_e32 v36, 0x42800000, v37
	v_mov_b32_e32 v35, 0
	v_cvt_pk_fp8_f32 v35, v29, v36
	ds_read2_b32 v[36:37], v150 offset1:32
	v_cvt_pk_fp8_f32 v34, v4, v15 op_sel:[0,0,1]
	s_waitcnt lgkmcnt(1)
	v_mul_f32_e32 v4, 0x42800000, v16
	v_mul_f32_e32 v15, 0x42800000, v17
	ds_read2_b32 v[16:17], v150 offset0:64 offset1:96
	v_cvt_pk_fp8_f32 v35, v4, v15 op_sel:[0,0,1]
	s_waitcnt lgkmcnt(1)
	v_mul_f32_e32 v4, 0x42800000, v36
	v_mul_f32_e32 v15, 0x42800000, v37
	v_mov_b32_e32 v36, 0
	v_cvt_pk_fp8_f32 v36, v4, v15
	s_waitcnt lgkmcnt(0)
; __device__ __forceinline__ MoeItem moe_item(const float* wg, const float* wu, const float* wd, const float* win, const float* wout, const float* wpn, const float* wpd, unsigned char* ws, int r, int lane) {
;     ...
;     const int mat = r / MOE_IE, q = r % MOE_IE, e = mat / 3, which = mat % 3, kb = q / 64, nb = q % 64, n0 = nb * 32;
;     const float* src = (which == 0 ? wg : (which == 1 ? wu : wd)) + (size_t)e * DM * DFF + (size_t)(kb * 128 + (lane >> 5)) * DFF + n0 + (lane & 31);
;     unsigned char* dst;
;     if (which < 2) dst = ws + WS_WGUT + ((size_t)(e * 16 + (n0 >> 7)) * 256 + which * 128 + (n0 & 127)) * DM;
;     else dst = ws + WS_WDT + ((size_t)e * DM + n0) * DFF;
;     MoeItem it; it.stride = DFF; it.dpitch = DM; it.src = src; it.dst = dst + kb * 128 + (size_t)(lane >> 3) * DM + 16 * (lane & 7); return it;
	v_mul_f32_e32 v4, 0x42800000, v16
	v_mul_f32_e32 v15, 0x42800000, v17
	ds_read2_b32 v[16:17], v150 offset0:192 offset1:224
	v_cvt_pk_fp8_f32 v36, v4, v15 op_sel:[0,0,1]
	v_mul_f32_e32 v4, 0x42800000, v38
	v_mul_f32_e32 v15, 0x42800000, v39
	v_mov_b32_e32 v37, 0
	v_cvt_pk_fp8_f32 v37, v4, v15
	s_waitcnt lgkmcnt(0)
	v_mul_f32_e32 v4, 0x42800000, v16
	v_mul_f32_e32 v15, 0x42800000, v17
	ds_read2_b32 v[16:17], v18 offset1:32
	v_cvt_pk_fp8_f32 v37, v4, v15 op_sel:[0,0,1]
	global_store_dwordx4 v[10:11], v[30:33], off sc0 sc1 nt
	ds_read2_b32 v[32:33], v18 offset0:64 offset1:96
	s_lshl_b64 s[38:39], s[38:39], 3
	s_waitcnt lgkmcnt(1)
	v_mul_f32_e32 v4, 0x42800000, v16
	v_mul_f32_e32 v15, 0x42800000, v17
	ds_read2_b32 v[16:17], v18 offset0:128 offset1:160
	v_mov_b32_e32 v30, 0
	v_cvt_pk_fp8_f32 v30, v4, v15
	s_waitcnt lgkmcnt(1)
	v_mul_f32_e32 v4, 0x42800000, v32
	v_mov_b32_e32 v31, 0
	s_waitcnt lgkmcnt(0)
	v_mul_f32_e32 v29, 0x42800000, v16
	v_mul_f32_e32 v32, 0x42800000, v17
	ds_read2_b32 v[16:17], v18 offset0:192 offset1:224
	v_mul_f32_e32 v15, 0x42800000, v33
	v_cvt_pk_fp8_f32 v31, v29, v32
	ds_read2_b32 v[32:33], v156 offset1:32
	v_cvt_pk_fp8_f32 v30, v4, v15 op_sel:[0,0,1]
	s_waitcnt lgkmcnt(1)
	v_mul_f32_e32 v4, 0x42800000, v16
	v_mul_f32_e32 v15, 0x42800000, v17
	ds_read2_b32 v[16:17], v156 offset0:64 offset1:96
	v_lshl_add_u64 v[10:11], v[10:11], 0, s[38:39]
	global_store_dwordx4 v[10:11], v[34:37], off sc0 sc1 nt
	ds_read2_b32 v[34:35], v156 offset0:128 offset1:160
	v_cvt_pk_fp8_f32 v31, v4, v15 op_sel:[0,0,1]
	s_waitcnt lgkmcnt(2)
	v_mul_f32_e32 v4, 0x42800000, v32
	v_mul_f32_e32 v15, 0x42800000, v33
	v_mov_b32_e32 v32, 0
	v_cvt_pk_fp8_f32 v32, v4, v15
	s_waitcnt lgkmcnt(1)
	v_mul_f32_e32 v4, 0x42800000, v16
	v_mul_f32_e32 v15, 0x42800000, v17
	ds_read2_b32 v[16:17], v156 offset0:192 offset1:224
	s_waitcnt lgkmcnt(1)
	v_mul_f32_e32 v29, 0x42800000, v34
	v_mul_f32_e32 v34, 0x42800000, v35
	v_mov_b32_e32 v33, 0
	v_cvt_pk_fp8_f32 v33, v29, v34
	ds_read2_b32 v[34:35], v19 offset1:32
	v_cvt_pk_fp8_f32 v32, v4, v15 op_sel:[0,0,1]
	s_waitcnt lgkmcnt(1)
	v_mul_f32_e32 v4, 0x42800000, v16
	v_mul_f32_e32 v15, 0x42800000, v17
	ds_read2_b32 v[16:17], v19 offset0:64 offset1:96
	ds_read2_b32 v[36:37], v19 offset0:128 offset1:160
	v_cvt_pk_fp8_f32 v33, v4, v15 op_sel:[0,0,1]
	s_waitcnt lgkmcnt(2)
	v_mul_f32_e32 v4, 0x42800000, v34
	v_mul_f32_e32 v15, 0x42800000, v35
	v_mov_b32_e32 v34, 0
	v_cvt_pk_fp8_f32 v34, v4, v15
	s_waitcnt lgkmcnt(1)
	v_mul_f32_e32 v4, 0x42800000, v16
	v_mul_f32_e32 v15, 0x42800000, v17
	ds_read2_b32 v[16:17], v19 offset0:192 offset1:224
	s_waitcnt lgkmcnt(1)
	v_mul_f32_e32 v29, 0x42800000, v36
	v_mul_f32_e32 v36, 0x42800000, v37
	v_mov_b32_e32 v35, 0
	v_add_u32_e32 v160, 0x400, v19
	v_cvt_pk_fp8_f32 v35, v29, v36
	ds_read2_b32 v[36:37], v160 offset1:32
	v_cvt_pk_fp8_f32 v34, v4, v15 op_sel:[0,0,1]
	s_waitcnt lgkmcnt(1)
	v_mul_f32_e32 v4, 0x42800000, v16
	v_mul_f32_e32 v15, 0x42800000, v17
	ds_read2_b32 v[16:17], v160 offset0:64 offset1:96
	ds_read2_b32 v[38:39], v160 offset0:128 offset1:160
	v_cvt_pk_fp8_f32 v35, v4, v15 op_sel:[0,0,1]
	s_waitcnt lgkmcnt(2)
	v_mul_f32_e32 v4, 0x42800000, v36
	v_mul_f32_e32 v15, 0x42800000, v37
	v_mov_b32_e32 v36, 0
	v_cvt_pk_fp8_f32 v36, v4, v15
	s_waitcnt lgkmcnt(1)
	v_mul_f32_e32 v4, 0x42800000, v16
	v_mul_f32_e32 v15, 0x42800000, v17
	ds_read2_b32 v[16:17], v160 offset0:192 offset1:224
	s_waitcnt lgkmcnt(1)
	v_mul_f32_e32 v29, 0x42800000, v38
	v_mul_f32_e32 v38, 0x42800000, v39
	v_mov_b32_e32 v37, 0
	v_cvt_pk_fp8_f32 v37, v29, v38
	v_cvt_pk_fp8_f32 v36, v4, v15 op_sel:[0,0,1]
	s_waitcnt lgkmcnt(0)
	v_mul_f32_e32 v4, 0x42800000, v16
	v_mul_f32_e32 v15, 0x42800000, v17
	v_cvt_pk_fp8_f32 v37, v4, v15 op_sel:[0,0,1]
	v_lshl_add_u64 v[10:11], v[10:11], 0, s[38:39]
	global_store_dwordx4 v[10:11], v[30:33], off sc0 sc1 nt
	v_lshl_add_u64 v[10:11], v[10:11], 0, s[38:39]
	global_store_dwordx4 v[10:11], v[34:37], off sc0 sc1 nt
	s_waitcnt lgkmcnt(0)
	s_add_i32 s3, s89, s3
	s_mov_b32 s96, 0
	s_min_i32 s43, s3, s7
	s_cmp_lt_i32 s43, 0x19000
	s_mov_b64 s[38:39], -1
	s_cbranch_scc0 .LBB0_126
	s_cmp_lt_i32 s43, 0x18c00
	s_cbranch_scc0 .LBB0_123
	s_cmp_lt_i32 s43, 0x18000
	s_cbranch_scc0 .LBB0_113
	s_mov_b32 s96, 1
	s_ashr_i32 s4, s43, 31
	s_lshr_b32 s4, s4, 22
	s_add_i32 s4, s43, s4
	s_ashr_i32 s39, s4, 10
	s_and_b32 s4, s4, 0xfc00
	s_sub_i32 s46, s43, s4
	s_mul_hi_i32 s4, s43, 0x2aaaaaab
	s_lshr_b32 s38, s4, 31
	s_ashr_i32 s4, s4, 9
	s_add_i32 s38, s4, s38
	s_mul_hi_i32 s4, s39, 0x55555556
	s_lshr_b32 s45, s4, 31
	s_add_i32 s4, s4, s45
	s_mul_i32 s4, s4, 3
	s_sub_i32 s4, s39, s4
	s_sext_i32_i16 s39, s46
	s_bfe_u32 s39, s39, 0x60019
	s_add_i32 s45, s46, s39
	s_and_b32 s39, s45, 0xffc0
	s_sub_i32 s39, s46, s39
	s_sext_i32_i16 s84, s39
	s_lshl_b32 s46, s84, 5
	s_ashr_i32 s39, s38, 31
	s_ashr_i32 s47, s46, 31
	s_cmp_gt_i32 s4, 1
	s_mov_b64 s[70:71], -1
	s_cbranch_scc0 .LBB0_110
	s_lshl_b64 s[68:69], s[38:39], 22
	s_lshl_b64 s[70:71], s[46:47], 11
	s_add_u32 s68, s73, s68
	s_addc_u32 s69, s74, s69
	s_add_u32 s68, s68, s70
	s_addc_u32 s69, s69, s71
	s_mov_b64 s[70:71], 0
